# scatter phase: 16 assignments per wave handled in two batches of 8 with all index/scale/row loads issued up front (was 3 dependent round trips per assignment)
# speedup vs baseline: 1.0098x; 1.0035x over previous
.LBB0_3761:
	s_ashr_i32 s9, s8, 31
	s_lshl_b64 s[12:13], s[8:9], 2
	s_add_u32 s30, s17, s12
	s_addc_u32 s31, s18, s13
	s_add_u32 s12, s19, s12
	s_addc_u32 s13, s20, s13
	s_ashr_i32 s11, s10, 31
	s_lshl_b64 s[98:99], s[10:11], 2
	s_add_u32 s98, s14, s98
	s_addc_u32 s99, s15, s99
	s_add_i32 s100, s16, s8
	s_ashr_i32 s101, s100, 31
	s_lshl_b64 s[100:101], s[100:101], 2
	s_add_u32 s100, s49, s100
	s_addc_u32 s101, s50, s101
	s_lshl_b64 s[10:11], s[10:11], 11
	v_lshl_add_u64 v[66:67], v[4:5], 0, s[10:11]
	s_mov_b64 s[28:29], 0x2000
	global_load_dword v8, v3, s[30:31] sc1
	global_load_dword v16, v3, s[12:13] sc1
	global_load_dword v24, v3, s[98:99] sc1
	global_load_dword v9, v3, s[30:31] offset:32 sc1
	global_load_dword v17, v3, s[12:13] offset:32 sc1
	global_load_dword v25, v3, s[98:99] offset:16 sc1
	global_load_dword v10, v3, s[30:31] offset:64 sc1
	global_load_dword v18, v3, s[12:13] offset:64 sc1
	global_load_dword v26, v3, s[98:99] offset:32 sc1
	global_load_dword v11, v3, s[30:31] offset:96 sc1
	global_load_dword v19, v3, s[12:13] offset:96 sc1
	global_load_dword v27, v3, s[98:99] offset:48 sc1
	global_load_dword v12, v3, s[30:31] offset:128 sc1
	global_load_dword v20, v3, s[12:13] offset:128 sc1
	global_load_dword v28, v3, s[98:99] offset:64 sc1
	global_load_dword v13, v3, s[30:31] offset:160 sc1
	global_load_dword v21, v3, s[12:13] offset:160 sc1
	global_load_dword v29, v3, s[98:99] offset:80 sc1
	global_load_dword v14, v3, s[30:31] offset:192 sc1
	global_load_dword v22, v3, s[12:13] offset:192 sc1
	global_load_dword v30, v3, s[98:99] offset:96 sc1
	global_load_dword v15, v3, s[30:31] offset:224 sc1
	global_load_dword v23, v3, s[12:13] offset:224 sc1
	global_load_dword v31, v3, s[98:99] offset:112 sc1
	global_load_dwordx4 v[80:83], v[66:67], off
	global_load_dwordx4 v[84:87], v[66:67], off offset:1024
	v_lshl_add_u64 v[66:67], v[66:67], 0, s[28:29]
	global_load_dwordx4 v[88:91], v[66:67], off
	global_load_dwordx4 v[92:95], v[66:67], off offset:1024
	v_lshl_add_u64 v[66:67], v[66:67], 0, s[28:29]
	global_load_dwordx4 v[96:99], v[66:67], off
	global_load_dwordx4 v[100:103], v[66:67], off offset:1024
	v_lshl_add_u64 v[66:67], v[66:67], 0, s[28:29]
	global_load_dwordx4 v[104:107], v[66:67], off
	global_load_dwordx4 v[108:111], v[66:67], off offset:1024
	v_lshl_add_u64 v[66:67], v[66:67], 0, s[28:29]
	global_load_dwordx4 v[112:115], v[66:67], off
	global_load_dwordx4 v[116:119], v[66:67], off offset:1024
	v_lshl_add_u64 v[66:67], v[66:67], 0, s[28:29]
	global_load_dwordx4 v[120:123], v[66:67], off
	global_load_dwordx4 v[124:127], v[66:67], off offset:1024
	v_lshl_add_u64 v[66:67], v[66:67], 0, s[28:29]
	global_load_dwordx4 v[128:131], v[66:67], off
	global_load_dwordx4 v[132:135], v[66:67], off offset:1024
	v_lshl_add_u64 v[66:67], v[66:67], 0, s[28:29]
	global_load_dwordx4 v[136:139], v[66:67], off
	global_load_dwordx4 v[140:143], v[66:67], off offset:1024
	v_lshl_add_u64 v[66:67], v[66:67], 0, s[28:29]
	s_waitcnt vmcnt(16)
	v_lshlrev_b32_e32 v1, 2, v8
	v_lshlrev_b32_e32 v8, 10, v8
	v_add_u32_e32 v8, s27, v8
	ds_read_b32 v32, v1 offset:8224
	ds_read_b32 v40, v8
	v_lshlrev_b32_e32 v1, 2, v9
	v_lshlrev_b32_e32 v9, 10, v9
	v_add_u32_e32 v9, s27, v9
	ds_read_b32 v33, v1 offset:8224
	ds_read_b32 v41, v9
	v_lshlrev_b32_e32 v1, 2, v10
	v_lshlrev_b32_e32 v10, 10, v10
	v_add_u32_e32 v10, s27, v10
	ds_read_b32 v34, v1 offset:8224
	ds_read_b32 v42, v10
	v_lshlrev_b32_e32 v1, 2, v11
	v_lshlrev_b32_e32 v11, 10, v11
	v_add_u32_e32 v11, s27, v11
	ds_read_b32 v35, v1 offset:8224
	ds_read_b32 v43, v11
	v_lshlrev_b32_e32 v1, 2, v12
	v_lshlrev_b32_e32 v12, 10, v12
	v_add_u32_e32 v12, s27, v12
	ds_read_b32 v36, v1 offset:8224
	ds_read_b32 v44, v12
	v_lshlrev_b32_e32 v1, 2, v13
	v_lshlrev_b32_e32 v13, 10, v13
	v_add_u32_e32 v13, s27, v13
	ds_read_b32 v37, v1 offset:8224
	ds_read_b32 v45, v13
	v_lshlrev_b32_e32 v1, 2, v14
	v_lshlrev_b32_e32 v14, 10, v14
	v_add_u32_e32 v14, s27, v14
	ds_read_b32 v38, v1 offset:8224
	ds_read_b32 v46, v14
	v_lshlrev_b32_e32 v1, 2, v15
	v_lshlrev_b32_e32 v15, 10, v15
	v_add_u32_e32 v15, s27, v15
	ds_read_b32 v39, v1 offset:8224
	ds_read_b32 v47, v15
	s_waitcnt lgkmcnt(0)
	v_lshlrev_b32_e32 v32, 8, v32
	v_add_u32_e32 v40, v40, v16
	v_add_u32_e32 v40, v40, v32
	v_lshlrev_b32_e32 v33, 8, v33
	v_add_u32_e32 v41, v41, v17
	v_add_u32_e32 v41, v41, v33
	v_lshlrev_b32_e32 v34, 8, v34
	v_add_u32_e32 v42, v42, v18
	v_add_u32_e32 v42, v42, v34
	v_lshlrev_b32_e32 v35, 8, v35
	v_add_u32_e32 v43, v43, v19
	v_add_u32_e32 v43, v43, v35
	v_lshlrev_b32_e32 v36, 8, v36
	v_add_u32_e32 v44, v44, v20
	v_add_u32_e32 v44, v44, v36
	v_lshlrev_b32_e32 v37, 8, v37
	v_add_u32_e32 v45, v45, v21
	v_add_u32_e32 v45, v45, v37
	v_lshlrev_b32_e32 v38, 8, v38
	v_add_u32_e32 v46, v46, v22
	v_add_u32_e32 v46, v46, v38
	v_lshlrev_b32_e32 v39, 8, v39
	v_add_u32_e32 v47, v47, v23
	v_add_u32_e32 v47, v47, v39
	v_lshlrev_b32_e32 v50, 2, v40
	v_mov_b32_e32 v51, 0
	v_lshl_add_u64 v[50:51], s[34:35], 0, v[50:51]
	v_lshlrev_b32_e32 v144, 11, v40
	v_mov_b32_e32 v145, 0
	v_lshl_add_u64 v[144:145], v[6:7], 0, v[144:145]
	v_lshlrev_b32_e32 v52, 2, v41
	v_mov_b32_e32 v53, 0
	v_lshl_add_u64 v[52:53], s[34:35], 0, v[52:53]
	v_lshlrev_b32_e32 v146, 11, v41
	v_mov_b32_e32 v147, 0
	v_lshl_add_u64 v[146:147], v[6:7], 0, v[146:147]
	v_lshlrev_b32_e32 v54, 2, v42
	v_mov_b32_e32 v55, 0
	v_lshl_add_u64 v[54:55], s[34:35], 0, v[54:55]
	v_lshlrev_b32_e32 v148, 11, v42
	v_mov_b32_e32 v149, 0
	v_lshl_add_u64 v[148:149], v[6:7], 0, v[148:149]
	v_lshlrev_b32_e32 v56, 2, v43
	v_mov_b32_e32 v57, 0
	v_lshl_add_u64 v[56:57], s[34:35], 0, v[56:57]
	v_lshlrev_b32_e32 v150, 11, v43
	v_mov_b32_e32 v151, 0
	v_lshl_add_u64 v[150:151], v[6:7], 0, v[150:151]
	v_lshlrev_b32_e32 v58, 2, v44
	v_mov_b32_e32 v59, 0
	v_lshl_add_u64 v[58:59], s[34:35], 0, v[58:59]
	v_lshlrev_b32_e32 v152, 11, v44
	v_mov_b32_e32 v153, 0
	v_lshl_add_u64 v[152:153], v[6:7], 0, v[152:153]
	v_lshlrev_b32_e32 v60, 2, v45
	v_mov_b32_e32 v61, 0
	v_lshl_add_u64 v[60:61], s[34:35], 0, v[60:61]
	v_lshlrev_b32_e32 v154, 11, v45
	v_mov_b32_e32 v155, 0
	v_lshl_add_u64 v[154:155], v[6:7], 0, v[154:155]
	v_lshlrev_b32_e32 v62, 2, v46
	v_mov_b32_e32 v63, 0
	v_lshl_add_u64 v[62:63], s[34:35], 0, v[62:63]
	v_lshlrev_b32_e32 v156, 11, v46
	v_mov_b32_e32 v157, 0
	v_lshl_add_u64 v[156:157], v[6:7], 0, v[156:157]
	v_lshlrev_b32_e32 v64, 2, v47
	v_mov_b32_e32 v65, 0
	v_lshl_add_u64 v[64:65], s[34:35], 0, v[64:65]
	v_lshlrev_b32_e32 v158, 11, v47
	v_mov_b32_e32 v159, 0
	v_lshl_add_u64 v[158:159], v[6:7], 0, v[158:159]
	s_and_saveexec_b64 s[8:9], s[0:1]
	global_store_dword v3, v40, s[100:101]
	global_store_dword v[50:51], v24, off
	global_store_dword v3, v41, s[100:101] offset:32
	global_store_dword v[52:53], v25, off
	global_store_dword v3, v42, s[100:101] offset:64
	global_store_dword v[54:55], v26, off
	global_store_dword v3, v43, s[100:101] offset:96
	global_store_dword v[56:57], v27, off
	global_store_dword v3, v44, s[100:101] offset:128
	global_store_dword v[58:59], v28, off
	global_store_dword v3, v45, s[100:101] offset:160
	global_store_dword v[60:61], v29, off
	global_store_dword v3, v46, s[100:101] offset:192
	global_store_dword v[62:63], v30, off
	global_store_dword v3, v47, s[100:101] offset:224
	global_store_dword v[64:65], v31, off
	s_or_b64 exec, exec, s[8:9]
	s_waitcnt vmcnt(30)
	global_store_dwordx4 v[144:145], v[80:83], off
	global_store_dwordx4 v[144:145], v[84:87], off offset:1024
	s_waitcnt vmcnt(30)
	global_store_dwordx4 v[146:147], v[88:91], off
	global_store_dwordx4 v[146:147], v[92:95], off offset:1024
	s_waitcnt vmcnt(30)
	global_store_dwordx4 v[148:149], v[96:99], off
	global_store_dwordx4 v[148:149], v[100:103], off offset:1024
	s_waitcnt vmcnt(30)
	global_store_dwordx4 v[150:151], v[104:107], off
	global_store_dwordx4 v[150:151], v[108:111], off offset:1024
	s_waitcnt vmcnt(30)
	global_store_dwordx4 v[152:153], v[112:115], off
	global_store_dwordx4 v[152:153], v[116:119], off offset:1024
	s_waitcnt vmcnt(30)
	global_store_dwordx4 v[154:155], v[120:123], off
	global_store_dwordx4 v[154:155], v[124:127], off offset:1024
	s_waitcnt vmcnt(30)
	global_store_dwordx4 v[156:157], v[128:131], off
	global_store_dwordx4 v[156:157], v[132:135], off offset:1024
	s_waitcnt vmcnt(30)
	global_store_dwordx4 v[158:159], v[136:139], off
	global_store_dwordx4 v[158:159], v[140:143], off offset:1024
	s_nop 1
	global_load_dword v8, v3, s[30:31] offset:256 sc1
	global_load_dword v16, v3, s[12:13] offset:256 sc1
	global_load_dword v24, v3, s[98:99] offset:128 sc1
	global_load_dword v9, v3, s[30:31] offset:288 sc1
	global_load_dword v17, v3, s[12:13] offset:288 sc1
	global_load_dword v25, v3, s[98:99] offset:144 sc1
	global_load_dword v10, v3, s[30:31] offset:320 sc1
	global_load_dword v18, v3, s[12:13] offset:320 sc1
	global_load_dword v26, v3, s[98:99] offset:160 sc1
	global_load_dword v11, v3, s[30:31] offset:352 sc1
	global_load_dword v19, v3, s[12:13] offset:352 sc1
	global_load_dword v27, v3, s[98:99] offset:176 sc1
	global_load_dword v12, v3, s[30:31] offset:384 sc1
	global_load_dword v20, v3, s[12:13] offset:384 sc1
	global_load_dword v28, v3, s[98:99] offset:192 sc1
	global_load_dword v13, v3, s[30:31] offset:416 sc1
	global_load_dword v21, v3, s[12:13] offset:416 sc1
	global_load_dword v29, v3, s[98:99] offset:208 sc1
	global_load_dword v14, v3, s[30:31] offset:448 sc1
	global_load_dword v22, v3, s[12:13] offset:448 sc1
	global_load_dword v30, v3, s[98:99] offset:224 sc1
	global_load_dword v15, v3, s[30:31] offset:480 sc1
	global_load_dword v23, v3, s[12:13] offset:480 sc1
	global_load_dword v31, v3, s[98:99] offset:240 sc1
	global_load_dwordx4 v[80:83], v[66:67], off
	global_load_dwordx4 v[84:87], v[66:67], off offset:1024
	v_lshl_add_u64 v[66:67], v[66:67], 0, s[28:29]
	global_load_dwordx4 v[88:91], v[66:67], off
	global_load_dwordx4 v[92:95], v[66:67], off offset:1024
	v_lshl_add_u64 v[66:67], v[66:67], 0, s[28:29]
	global_load_dwordx4 v[96:99], v[66:67], off
	global_load_dwordx4 v[100:103], v[66:67], off offset:1024
	v_lshl_add_u64 v[66:67], v[66:67], 0, s[28:29]
	global_load_dwordx4 v[104:107], v[66:67], off
	global_load_dwordx4 v[108:111], v[66:67], off offset:1024
	v_lshl_add_u64 v[66:67], v[66:67], 0, s[28:29]
	global_load_dwordx4 v[112:115], v[66:67], off
	global_load_dwordx4 v[116:119], v[66:67], off offset:1024
	v_lshl_add_u64 v[66:67], v[66:67], 0, s[28:29]
	global_load_dwordx4 v[120:123], v[66:67], off
	global_load_dwordx4 v[124:127], v[66:67], off offset:1024
	v_lshl_add_u64 v[66:67], v[66:67], 0, s[28:29]
	global_load_dwordx4 v[128:131], v[66:67], off
	global_load_dwordx4 v[132:135], v[66:67], off offset:1024
	v_lshl_add_u64 v[66:67], v[66:67], 0, s[28:29]
	global_load_dwordx4 v[136:139], v[66:67], off
	global_load_dwordx4 v[140:143], v[66:67], off offset:1024
	v_lshl_add_u64 v[66:67], v[66:67], 0, s[28:29]
	s_waitcnt vmcnt(16)
	v_lshlrev_b32_e32 v1, 2, v8
	v_lshlrev_b32_e32 v8, 10, v8
	v_add_u32_e32 v8, s27, v8
	ds_read_b32 v32, v1 offset:8224
	ds_read_b32 v40, v8
	v_lshlrev_b32_e32 v1, 2, v9
	v_lshlrev_b32_e32 v9, 10, v9
	v_add_u32_e32 v9, s27, v9
	ds_read_b32 v33, v1 offset:8224
	ds_read_b32 v41, v9
	v_lshlrev_b32_e32 v1, 2, v10
	v_lshlrev_b32_e32 v10, 10, v10
	v_add_u32_e32 v10, s27, v10
	ds_read_b32 v34, v1 offset:8224
	ds_read_b32 v42, v10
	v_lshlrev_b32_e32 v1, 2, v11
	v_lshlrev_b32_e32 v11, 10, v11
	v_add_u32_e32 v11, s27, v11
	ds_read_b32 v35, v1 offset:8224
	ds_read_b32 v43, v11
	v_lshlrev_b32_e32 v1, 2, v12
	v_lshlrev_b32_e32 v12, 10, v12
	v_add_u32_e32 v12, s27, v12
	ds_read_b32 v36, v1 offset:8224
	ds_read_b32 v44, v12
	v_lshlrev_b32_e32 v1, 2, v13
	v_lshlrev_b32_e32 v13, 10, v13
	v_add_u32_e32 v13, s27, v13
	ds_read_b32 v37, v1 offset:8224
	ds_read_b32 v45, v13
	v_lshlrev_b32_e32 v1, 2, v14
	v_lshlrev_b32_e32 v14, 10, v14
	v_add_u32_e32 v14, s27, v14
	ds_read_b32 v38, v1 offset:8224
	ds_read_b32 v46, v14
	v_lshlrev_b32_e32 v1, 2, v15
	v_lshlrev_b32_e32 v15, 10, v15
	v_add_u32_e32 v15, s27, v15
	ds_read_b32 v39, v1 offset:8224
	ds_read_b32 v47, v15
	s_waitcnt lgkmcnt(0)
	v_lshlrev_b32_e32 v32, 8, v32
	v_add_u32_e32 v40, v40, v16
	v_add_u32_e32 v40, v40, v32
	v_lshlrev_b32_e32 v33, 8, v33
	v_add_u32_e32 v41, v41, v17
	v_add_u32_e32 v41, v41, v33
	v_lshlrev_b32_e32 v34, 8, v34
	v_add_u32_e32 v42, v42, v18
	v_add_u32_e32 v42, v42, v34
	v_lshlrev_b32_e32 v35, 8, v35
	v_add_u32_e32 v43, v43, v19
	v_add_u32_e32 v43, v43, v35
	v_lshlrev_b32_e32 v36, 8, v36
	v_add_u32_e32 v44, v44, v20
	v_add_u32_e32 v44, v44, v36
	v_lshlrev_b32_e32 v37, 8, v37
	v_add_u32_e32 v45, v45, v21
	v_add_u32_e32 v45, v45, v37
	v_lshlrev_b32_e32 v38, 8, v38
	v_add_u32_e32 v46, v46, v22
	v_add_u32_e32 v46, v46, v38
	v_lshlrev_b32_e32 v39, 8, v39
	v_add_u32_e32 v47, v47, v23
	v_add_u32_e32 v47, v47, v39
	v_lshlrev_b32_e32 v50, 2, v40
	v_mov_b32_e32 v51, 0
	v_lshl_add_u64 v[50:51], s[34:35], 0, v[50:51]
	v_lshlrev_b32_e32 v144, 11, v40
	v_mov_b32_e32 v145, 0
	v_lshl_add_u64 v[144:145], v[6:7], 0, v[144:145]
	v_lshlrev_b32_e32 v52, 2, v41
	v_mov_b32_e32 v53, 0
	v_lshl_add_u64 v[52:53], s[34:35], 0, v[52:53]
	v_lshlrev_b32_e32 v146, 11, v41
	v_mov_b32_e32 v147, 0
	v_lshl_add_u64 v[146:147], v[6:7], 0, v[146:147]
	v_lshlrev_b32_e32 v54, 2, v42
	v_mov_b32_e32 v55, 0
	v_lshl_add_u64 v[54:55], s[34:35], 0, v[54:55]
	v_lshlrev_b32_e32 v148, 11, v42
	v_mov_b32_e32 v149, 0
	v_lshl_add_u64 v[148:149], v[6:7], 0, v[148:149]
	v_lshlrev_b32_e32 v56, 2, v43
	v_mov_b32_e32 v57, 0
	v_lshl_add_u64 v[56:57], s[34:35], 0, v[56:57]
	v_lshlrev_b32_e32 v150, 11, v43
	v_mov_b32_e32 v151, 0
	v_lshl_add_u64 v[150:151], v[6:7], 0, v[150:151]
	v_lshlrev_b32_e32 v58, 2, v44
	v_mov_b32_e32 v59, 0
	v_lshl_add_u64 v[58:59], s[34:35], 0, v[58:59]
	v_lshlrev_b32_e32 v152, 11, v44
	v_mov_b32_e32 v153, 0
	v_lshl_add_u64 v[152:153], v[6:7], 0, v[152:153]
	v_lshlrev_b32_e32 v60, 2, v45
	v_mov_b32_e32 v61, 0
	v_lshl_add_u64 v[60:61], s[34:35], 0, v[60:61]
	v_lshlrev_b32_e32 v154, 11, v45
	v_mov_b32_e32 v155, 0
	v_lshl_add_u64 v[154:155], v[6:7], 0, v[154:155]
	v_lshlrev_b32_e32 v62, 2, v46
	v_mov_b32_e32 v63, 0
	v_lshl_add_u64 v[62:63], s[34:35], 0, v[62:63]
	v_lshlrev_b32_e32 v156, 11, v46
	v_mov_b32_e32 v157, 0
	v_lshl_add_u64 v[156:157], v[6:7], 0, v[156:157]
	v_lshlrev_b32_e32 v64, 2, v47
	v_mov_b32_e32 v65, 0
	v_lshl_add_u64 v[64:65], s[34:35], 0, v[64:65]
	v_lshlrev_b32_e32 v158, 11, v47
	v_mov_b32_e32 v159, 0
	v_lshl_add_u64 v[158:159], v[6:7], 0, v[158:159]
	s_and_saveexec_b64 s[8:9], s[0:1]
	global_store_dword v3, v40, s[100:101] offset:256
	global_store_dword v[50:51], v24, off
	global_store_dword v3, v41, s[100:101] offset:288
	global_store_dword v[52:53], v25, off
	global_store_dword v3, v42, s[100:101] offset:320
	global_store_dword v[54:55], v26, off
	global_store_dword v3, v43, s[100:101] offset:352
	global_store_dword v[56:57], v27, off
	global_store_dword v3, v44, s[100:101] offset:384
	global_store_dword v[58:59], v28, off
	global_store_dword v3, v45, s[100:101] offset:416
	global_store_dword v[60:61], v29, off
	global_store_dword v3, v46, s[100:101] offset:448
	global_store_dword v[62:63], v30, off
	global_store_dword v3, v47, s[100:101] offset:480
	global_store_dword v[64:65], v31, off
	s_or_b64 exec, exec, s[8:9]
	s_waitcnt vmcnt(30)
	global_store_dwordx4 v[144:145], v[80:83], off
	global_store_dwordx4 v[144:145], v[84:87], off offset:1024
	s_waitcnt vmcnt(30)
	global_store_dwordx4 v[146:147], v[88:91], off
	global_store_dwordx4 v[146:147], v[92:95], off offset:1024
	s_waitcnt vmcnt(30)
	global_store_dwordx4 v[148:149], v[96:99], off
	global_store_dwordx4 v[148:149], v[100:103], off offset:1024
	s_waitcnt vmcnt(30)
	global_store_dwordx4 v[150:151], v[104:107], off
	global_store_dwordx4 v[150:151], v[108:111], off offset:1024
	s_waitcnt vmcnt(30)
	global_store_dwordx4 v[152:153], v[112:115], off
	global_store_dwordx4 v[152:153], v[116:119], off offset:1024
	s_waitcnt vmcnt(30)
	global_store_dwordx4 v[154:155], v[120:123], off
	global_store_dwordx4 v[154:155], v[124:127], off offset:1024
	s_waitcnt vmcnt(30)
	global_store_dwordx4 v[156:157], v[128:131], off
	global_store_dwordx4 v[156:157], v[132:135], off offset:1024
	s_waitcnt vmcnt(30)
	global_store_dwordx4 v[158:159], v[136:139], off
	global_store_dwordx4 v[158:159], v[140:143], off offset:1024
	s_branch .LBB0_3757

	.amdhsa_kernel _Z10fwd_kernel4Args
		.amdhsa_group_segment_fixed_size 0
		.amdhsa_private_segment_fixed_size 0
		.amdhsa_kernarg_size 456
		.amdhsa_user_sgpr_count 2
		.amdhsa_user_sgpr_dispatch_ptr 0
		.amdhsa_user_sgpr_queue_ptr 0
		.amdhsa_user_sgpr_kernarg_segment_ptr 1
		.amdhsa_user_sgpr_dispatch_id 0
		.amdhsa_user_sgpr_kernarg_preload_length 0
		.amdhsa_user_sgpr_kernarg_preload_offset 0
		.amdhsa_user_sgpr_private_segment_size 0
		.amdhsa_uses_dynamic_stack 0
		.amdhsa_enable_private_segment 0
		.amdhsa_system_sgpr_workgroup_id_x 1
		.amdhsa_system_sgpr_workgroup_id_y 0
		.amdhsa_system_sgpr_workgroup_id_z 0
		.amdhsa_system_sgpr_workgroup_info 0
		.amdhsa_system_vgpr_workitem_id 0
		.amdhsa_next_free_vgpr 256
		.amdhsa_next_free_sgpr 102
		.amdhsa_accum_offset 256
		.amdhsa_reserve_vcc 1
		.amdhsa_float_round_mode_32 0
		.amdhsa_float_round_mode_16_64 0
		.amdhsa_float_denorm_mode_32 3
		.amdhsa_float_denorm_mode_16_64 3
		.amdhsa_dx10_clamp 1
		.amdhsa_ieee_mode 1
		.amdhsa_fp16_overflow 0
		.amdhsa_tg_split 0
		.amdhsa_exception_fp_ieee_invalid_op 0
		.amdhsa_exception_fp_denorm_src 0
		.amdhsa_exception_fp_ieee_div_zero 0
		.amdhsa_exception_fp_ieee_overflow 0
		.amdhsa_exception_fp_ieee_underflow 0
		.amdhsa_exception_fp_ieee_inexact 0
		.amdhsa_exception_int_div_zero 0
	.end_amdhsa_kernel

amdhsa.kernels:
  - .agpr_count:     0
    .args:
      - .offset:         0
        .size:           200
        .value_kind:     by_value
      - .offset:         200
        .size:           4
        .value_kind:     hidden_block_count_x
      - .offset:         204
        .size:           4
        .value_kind:     hidden_block_count_y
      - .offset:         208
        .size:           4
        .value_kind:     hidden_block_count_z
      - .offset:         212
        .size:           2
        .value_kind:     hidden_group_size_x
      - .offset:         214
        .size:           2
        .value_kind:     hidden_group_size_y
      - .offset:         216
        .size:           2
        .value_kind:     hidden_group_size_z
      - .offset:         218
        .size:           2
        .value_kind:     hidden_remainder_x
      - .offset:         220
        .size:           2
        .value_kind:     hidden_remainder_y
      - .offset:         222
        .size:           2
        .value_kind:     hidden_remainder_z
      - .offset:         240
        .size:           8
        .value_kind:     hidden_global_offset_x
      - .offset:         248
        .size:           8
        .value_kind:     hidden_global_offset_y
      - .offset:         256
        .size:           8
        .value_kind:     hidden_global_offset_z
      - .offset:         264
        .size:           2
        .value_kind:     hidden_grid_dims
      - .offset:         320
        .size:           4
        .value_kind:     hidden_dynamic_lds_size
    .group_segment_fixed_size: 0
    .kernarg_segment_align: 8
    .kernarg_segment_size: 456
    .language:       OpenCL C
    .language_version:
      - 2
      - 0
    .max_flat_workgroup_size: 512
    .name:           _Z10fwd_kernel4Args
    .private_segment_fixed_size: 0
    .sgpr_count:     108
    .sgpr_spill_count: 129
    .symbol:         _Z10fwd_kernel4Args.kd
    .uniform_work_group_size: 1
    .uses_dynamic_stack: false
    .vgpr_count:     256
    .vgpr_spill_count: 0
    .wavefront_size: 64
